# code prefetch sites: kernel entry 64KiB + P0 stage exits + arrivals (waves 4..7) + phase starts; prefetch dest in a0, v250 = tid*64 reserved
# speedup vs baseline: 1.0078x; 1.0009x over previous
_Z4mega5MArgs:
	v_lshlrev_b32_e32 v250, 6, v0
	v_lshlrev_b32_e32 v251, 7, v0
	s_getpc_b64 s[100:101]
	global_load_dword a0, v251, s[100:101]
	s_load_dwordx4 s[28:31], s[0:1], 0xe0
	s_load_dword s33, s[0:1], 0xf0
	s_add_u32 s4, s0, 0xf0
	s_addc_u32 s5, s1, 0
	v_lshrrev_b32_e32 v1, 6, v0
	s_nop 1
	v_readfirstlane_b32 s98, v1
	v_and_b32_e32 v1, 63, v0
	v_writelane_b32 v249, s4, 0
	v_cmp_eq_u32_e32 vcc, 0, v1
	s_nop 0
	v_writelane_b32 v249, s5, 1
	s_and_saveexec_b64 s[4:5], vcc
	s_cbranch_execz .LBB0_2
	s_getreg_b32 s3, hwreg(HW_REG_HW_ID, 0, 6)
	s_lshl_b32 s3, s3, 2
	s_and_b32 s3, s3, 0xfc
	s_add_i32 s3, s3, 0
	s_add_i32 s3, s3, 0x25c00
	v_lshrrev_b32_e32 v1, 6, v0
	v_mov_b32_e32 v2, s3
	ds_write_b32 v2, v1

.LBB0_39:
	s_getpc_b64 s[100:101]
	global_load_dword a0, v250, s[100:101]
	s_or_b64 exec, exec, s[6:7]
	v_lshl_add_u32 v0, s2, 9, v28
	s_mov_b32 s0, 0x20000
	s_lshl_b32 s6, s33, 9
	v_readlane_b32 s48, v249, 6
	v_readlane_b32 s49, v249, 7
	v_mov_b32_e32 v44, v0
	v_min_i32_e32 v45, 0x7ffff, v44
	v_lshrrev_b32_e32 v45, 5, v45
	v_lshlrev_b32_e32 v45, 2, v45
	s_nop 1
	global_load_dword v40, v45, s[48:49]
	v_add_u32_e32 v44, s6, v44
	v_min_i32_e32 v45, 0x7ffff, v44
	v_lshrrev_b32_e32 v45, 5, v45
	v_lshlrev_b32_e32 v45, 2, v45
	global_load_dword v41, v45, s[48:49]
	v_add_u32_e32 v44, s6, v44
	v_min_i32_e32 v45, 0x7ffff, v44
	v_lshrrev_b32_e32 v45, 5, v45
	v_lshlrev_b32_e32 v45, 2, v45
	global_load_dword v42, v45, s[48:49]
	v_add_u32_e32 v44, s6, v44
	v_min_i32_e32 v45, 0x7ffff, v44
	v_lshrrev_b32_e32 v45, 5, v45
	v_lshlrev_b32_e32 v45, 2, v45
	global_load_dword v43, v45, s[48:49]
	s_mov_b32 s99, 0
	v_cmp_gt_i32_e32 vcc, s0, v0
	s_and_saveexec_b64 s[0:1], vcc
	s_cbranch_execz .LBB0_44
	v_readlane_b32 s8, v249, 35
	v_readlane_b32 s9, v249, 36
	v_readlane_b32 s10, v249, 37
	v_readlane_b32 s11, v249, 38
	v_ashrrev_i32_e32 v1, 31, v0
	v_readlane_b32 s12, v249, 39
	v_readlane_b32 s13, v249, 40
	v_mov_b32_e32 v2, s8
	v_mov_b32_e32 v3, s9
	s_ashr_i32 s7, s6, 31
	v_lshl_add_u64 v[4:5], v[0:1], 1, s[78:79]
	s_mov_b64 s[10:11], 0x500000
	v_and_b32_e32 v6, 0x7f, v28
	v_lshl_add_u64 v[2:3], v[0:1], 2, v[2:3]
	s_lshl_b64 s[8:9], s[6:7], 2
	v_lshl_add_u64 v[4:5], v[4:5], 0, s[10:11]
	s_lshl_b64 s[10:11], s[6:7], 1
	s_mov_b64 s[12:13], 0
	s_movk_i32 s5, 0x7fff
	s_mov_b32 s7, 0x1ffff
	v_mov_b32_e32 v1, v0
	v_readlane_b32 s14, v249, 41
	v_readlane_b32 s15, v249, 42
	v_readlane_b32 s16, v249, 43
	v_readlane_b32 s17, v249, 44
	v_readlane_b32 s18, v249, 45
	v_readlane_b32 s19, v249, 46
	v_readlane_b32 s20, v249, 47
	v_readlane_b32 s21, v249, 48
	v_readlane_b32 s22, v249, 49
	v_readlane_b32 s23, v249, 50
	s_branch .LBB0_42

.LBB0_44:
	s_getpc_b64 s[100:101]
	global_load_dword a0, v250, s[100:101]
	s_or_b64 exec, exec, s[0:1]
	s_mov_b32 s0, 0x12000
	v_cmp_gt_i32_e32 vcc, s0, v0
	s_and_saveexec_b64 s[8:9], vcc
	s_cbranch_execz .LBB0_56
	v_cvt_f32_u32_e32 v2, s6
	v_add_u32_e32 v1, s6, v0
	v_mov_b32_e32 v3, s6
	v_cmp_gt_i32_e32 vcc, s0, v1
	v_rcp_iflag_f32_e32 v2, v2
	s_add_u32 s10, s78, 0x1200000
	v_addc_co_u32_e64 v3, s[0:1], v0, v3, vcc
	v_mul_f32_e32 v2, 0x4f7ffffe, v2
	v_cvt_u32_f32_e32 v2, v2
	s_addc_u32 s11, s79, 0
	v_max_i32_e32 v4, 0x12000, v1
	s_sub_i32 s0, 0, s6
	v_sub_u32_e32 v3, v4, v3
	v_mul_lo_u32 v4, s0, v2
	v_mul_hi_u32 v4, v2, v4
	v_add_u32_e32 v2, v2, v4
	v_mul_hi_u32 v2, v3, v2
	v_mul_lo_u32 v4, v2, s6
	v_sub_u32_e32 v3, v3, v4
	v_add_u32_e32 v4, 1, v2
	v_cmp_le_u32_e64 s[0:1], s6, v3
	s_mov_b64 s[12:13], -1
	s_nop 0
	v_cndmask_b32_e64 v2, v2, v4, s[0:1]
	v_subrev_u32_e32 v4, s6, v3
	v_cndmask_b32_e64 v3, v3, v4, s[0:1]
	v_add_u32_e32 v4, 1, v2
	v_cmp_le_u32_e64 s[0:1], s6, v3
	s_nop 1
	v_cndmask_b32_e64 v2, v2, v4, s[0:1]
	v_addc_co_u32_e32 v6, vcc, 1, v2, vcc
	v_cmp_lt_u32_e32 vcc, 1, v6
	v_mov_b32_e32 v2, v0
	s_and_saveexec_b64 s[0:1], vcc
	s_cbranch_execz .LBB0_49
	v_and_b32_e32 v7, -2, v6
	s_lshl_b32 s5, s33, 10
	v_readlane_b32 s48, v249, 35
	s_mov_b32 s7, s5
	s_mov_b64 s[12:13], 0
	s_mov_b32 s14, 0x38e38e39
	v_mov_b32_e32 v3, 0
	v_mov_b32_e32 v8, v7
	v_mov_b64_e32 v[4:5], v[0:1]
	v_readlane_b32 s56, v249, 43
	v_readlane_b32 s57, v249, 44
	v_readlane_b32 s60, v249, 47
	v_readlane_b32 s61, v249, 48
	v_readlane_b32 s49, v249, 36
	v_readlane_b32 s50, v249, 37
	v_readlane_b32 s51, v249, 38
	v_readlane_b32 s52, v249, 39
	v_readlane_b32 s53, v249, 40
	v_readlane_b32 s54, v249, 41
	v_readlane_b32 s55, v249, 42
	v_readlane_b32 s58, v249, 45
	v_readlane_b32 s59, v249, 46
	v_readlane_b32 s62, v249, 49
	v_readlane_b32 s63, v249, 50

.LBB0_49:
	s_getpc_b64 s[100:101]
	global_load_dword a0, v250, s[100:101]
	s_or_b64 exec, exec, s[0:1]
	s_and_b64 exec, exec, s[12:13]
	s_cbranch_execz .LBB0_56
	s_mov_b64 s[0:1], 0
	s_mov_b32 s5, 0x38e38e39
	v_mov_b32_e32 v5, 0
	s_mov_b32 s7, 0x11fff
	s_branch .LBB0_52

.LBB0_56:
	s_getpc_b64 s[100:101]
	global_load_dword a0, v250, s[100:101]
	s_or_b64 exec, exec, s[8:9]
	s_mov_b32 s0, 0x80000
	v_cmp_gt_i32_e32 vcc, s0, v0
	s_and_saveexec_b64 s[8:9], vcc
	s_cbranch_execz .LBB0_63
	s_add_u32 s10, s78, 0x100000
	s_addc_u32 s11, s79, 0
	s_add_u32 s12, s78, 0x300000
	v_and_b32_e32 v4, 31, v28
	s_mov_b32 s16, 0x24115d99
	s_mov_b32 s18, 0x6dc9c883
	s_addc_u32 s13, s79, 0
	v_cmp_ne_u32_e32 vcc, 0, v4
	s_mov_b64 s[14:15], 0
	s_mov_b32 s17, 0x3fe7ff22
	s_mov_b32 s19, 0x3fc45f30
	s_mov_b32 s5, 0x7ffff
	v_mov_b64_e32 v[14:15], 1.0
	s_and_saveexec_b64 s[20:21], vcc
	s_cbranch_execz .Lrope_f_done
	s_mov_b64 s[22:23], 0
	v_mov_b32_e32 v1, v4

.LBB0_72:
	s_getpc_b64 s[100:101]
	global_load_dword a0, v250, s[100:101]
	s_or_b64 exec, exec, s[0:1]
	s_waitcnt lgkmcnt(0)
	s_mov_b32 s0, s98
	v_mbcnt_lo_u32_b32 v0, -1, 0
	v_mbcnt_hi_u32_b32 v0, -1, v0
	s_nop 1
	v_lshl_add_u32 v0, s0, 6, v0
	s_nop 0
	v_cmp_eq_u32_e32 vcc, 0, v0
	s_and_saveexec_b64 s[0:1], vcc
	s_cbranch_execz .LBB0_74
	s_waitcnt vmcnt(0)
	buffer_inv sc1
	s_waitcnt vmcnt(0)

.LBB0_89:
	s_getpc_b64 s[100:101]
	global_load_dword a0, v250, s[100:101]
	s_or_b64 exec, exec, s[6:7]
.LBB0_90:
	s_cmp_lt_i32 s28, 2
	s_cselect_b64 s[0:1], -1, 0
	s_cmp_gt_i32 s29, 2
	s_cselect_b64 s[4:5], -1, 0
	s_and_b64 s[0:1], s[0:1], s[4:5]
	s_andn2_b64 vcc, exec, s[0:1]
	s_cbranch_vccnz .LBB0_240
	s_waitcnt vmcnt(0)
	s_barrier
	s_cmp_lt_u32 s98, 4
	s_cbranch_scc1 .Lipf_a7
	s_getpc_b64 s[100:101]
	v_lshlrev_b32_e32 v251, 1, v250
	v_add_u32_e32 v251, 0xffff8000, v251
	global_load_dword a0, v251, s[100:101]

.LBB0_239:
	s_or_b64 exec, exec, s[0:1]
	s_barrier
	s_getpc_b64 s[100:101]
	global_load_dword a0, v250, s[100:101]

.LBB0_381:
	s_cmp_gt_i32 s29, 3
	s_cselect_b64 s[4:5], -1, 0
	s_and_b64 s[0:1], s[6:7], s[4:5]
	s_andn2_b64 vcc, exec, s[0:1]
	s_cbranch_vccnz .LBB0_531
	s_waitcnt vmcnt(0)
	s_waitcnt lgkmcnt(0)
	s_barrier
	s_cmp_lt_u32 s98, 4
	s_cbranch_scc1 .Lipf_a9
	s_getpc_b64 s[100:101]
	v_lshlrev_b32_e32 v251, 1, v250
	v_add_u32_e32 v251, 0xffff8000, v251
	global_load_dword a0, v251, s[100:101]

.LBB0_561:
	v_readlane_b32 s4, v249, 51
	v_readlane_b32 s5, v249, 52
	v_readlane_b32 s6, v249, 53
	v_readlane_b32 s7, v249, 54
	s_cmp_gt_i32 s5, 4
	s_cselect_b64 s[6:7], -1, 0
	s_and_b64 s[0:1], s[84:85], s[6:7]
	s_andn2_b64 vcc, exec, s[0:1]
	s_cbranch_vccnz .LBB0_711
	s_waitcnt vmcnt(0)
	s_waitcnt lgkmcnt(0)
	s_barrier
	s_cmp_lt_u32 s98, 4
	s_cbranch_scc1 .Lipf_a11
	s_getpc_b64 s[100:101]
	v_lshlrev_b32_e32 v251, 1, v250
	v_add_u32_e32 v251, 0xffff8000, v251
	global_load_dword a0, v251, s[100:101]

.LBB0_732:
	s_cmp_gt_i32 s41, 5
	s_cselect_b64 s[12:13], -1, 0
	s_and_b64 s[0:1], s[8:9], s[12:13]
	s_andn2_b64 vcc, exec, s[0:1]
	s_cbranch_vccnz .LBB0_890
	s_waitcnt vmcnt(0)
	s_waitcnt lgkmcnt(0)
	s_barrier
	s_cmp_lt_u32 s98, 4
	s_cbranch_scc1 .Lipf_a13
	s_getpc_b64 s[100:101]
	v_lshlrev_b32_e32 v251, 1, v250
	v_add_u32_e32 v251, 0xffff8000, v251
	global_load_dword a0, v251, s[100:101]

.LBB0_923:
	s_cmp_gt_i32 s41, 6
	s_cselect_b64 s[4:5], -1, 0
	s_and_b64 s[0:1], s[14:15], s[4:5]
	s_andn2_b64 vcc, exec, s[0:1]
	s_cbranch_vccnz .LBB0_1075
	s_waitcnt vmcnt(0)
	s_waitcnt lgkmcnt(0)
	s_barrier
	s_cmp_lt_u32 s98, 4
	s_cbranch_scc1 .Lipf_a15
	s_getpc_b64 s[100:101]
	v_lshlrev_b32_e32 v251, 1, v250
	v_add_u32_e32 v251, 0xffff8000, v251
	global_load_dword a0, v251, s[100:101]

.LBB0_1440:
	v_readlane_b32 s48, v249, 51
	v_readlane_b32 s49, v249, 52
	s_cmp_lt_i32 s48, 8
	s_cselect_b64 s[0:1], -1, 0
	s_cmp_gt_i32 s49, 8
	s_cselect_b64 s[4:5], -1, 0
	s_and_b64 s[0:1], s[0:1], s[4:5]
	s_andn2_b64 vcc, exec, s[0:1]
	v_readlane_b32 s50, v249, 53
	v_readlane_b32 s51, v249, 54
	s_cbranch_vccnz .LBB0_1590
	s_waitcnt vmcnt(0)
	s_waitcnt vmcnt(0) lgkmcnt(0)
	s_barrier
	s_cmp_lt_u32 s98, 4
	s_cbranch_scc1 .Lipf_a17
	s_getpc_b64 s[100:101]
	v_lshlrev_b32_e32 v251, 1, v250
	v_add_u32_e32 v251, 0xffff8000, v251
	global_load_dword a0, v251, s[100:101]

.LBB0_1603:
	s_cmp_gt_i32 s49, 9
	s_cselect_b64 s[4:5], -1, 0
	s_and_b64 s[0:1], s[6:7], s[4:5]
	s_andn2_b64 vcc, exec, s[0:1]
	s_cbranch_vccnz .LBB0_1753
	s_waitcnt vmcnt(0)
	s_waitcnt vmcnt(0) lgkmcnt(0)
	s_barrier
	s_cmp_lt_u32 s98, 4
	s_cbranch_scc1 .Lipf_a19
	s_getpc_b64 s[100:101]
	v_lshlrev_b32_e32 v251, 1, v250
	v_add_u32_e32 v251, 0xffff8000, v251
	global_load_dword a0, v251, s[100:101]

.LBB0_1808:
	s_cmp_gt_i32 s49, 10
	s_cselect_b64 s[4:5], -1, 0
	s_and_b64 s[0:1], s[10:11], s[4:5]
	s_andn2_b64 vcc, exec, s[0:1]
	s_cbranch_vccnz .LBB0_1958
	s_waitcnt vmcnt(0)
	s_waitcnt vmcnt(0) lgkmcnt(0)
	s_barrier
	s_cmp_lt_u32 s98, 4
	s_cbranch_scc1 .Lipf_a21
	s_getpc_b64 s[100:101]
	v_lshlrev_b32_e32 v251, 1, v250
	v_add_u32_e32 v251, 0xffff8000, v251
	global_load_dword a0, v251, s[100:101]

.LBB0_1973:
	s_cmp_gt_i32 s49, 11
	s_cselect_b64 s[6:7], -1, 0
	s_and_b64 s[0:1], s[10:11], s[6:7]
	s_andn2_b64 vcc, exec, s[0:1]
	s_cbranch_vccnz .LBB0_2123
	s_waitcnt vmcnt(0)
	s_waitcnt vmcnt(0) lgkmcnt(0)
	s_barrier
	s_cmp_lt_u32 s98, 4
	s_cbranch_scc1 .Lipf_a23
	s_getpc_b64 s[100:101]
	v_lshlrev_b32_e32 v251, 1, v250
	v_add_u32_e32 v251, 0xffff8000, v251
	global_load_dword a0, v251, s[100:101]

.LBB0_2144:
	s_cmp_gt_i32 s49, 12
	s_cselect_b64 s[12:13], -1, 0
	s_and_b64 s[0:1], s[10:11], s[12:13]
	s_andn2_b64 vcc, exec, s[0:1]
	s_cbranch_vccnz .LBB0_2302
	s_waitcnt vmcnt(0)
	s_waitcnt vmcnt(0) lgkmcnt(0)
	s_barrier
	s_cmp_lt_u32 s98, 4
	s_cbranch_scc1 .Lipf_a25
	s_getpc_b64 s[100:101]
	v_lshlrev_b32_e32 v251, 1, v250
	v_add_u32_e32 v251, 0xffff8000, v251
	global_load_dword a0, v251, s[100:101]

.LBB0_2335:
	s_cmp_gt_i32 s49, 13
	s_cselect_b64 s[4:5], -1, 0
	s_and_b64 s[0:1], s[14:15], s[4:5]
	s_andn2_b64 vcc, exec, s[0:1]
	s_cbranch_vccnz .LBB0_2397
	s_waitcnt vmcnt(0)
	s_waitcnt vmcnt(0) lgkmcnt(0)
	s_barrier
	s_cmp_lt_u32 s98, 4
	s_cbranch_scc1 .Lipf_a27
	s_getpc_b64 s[100:101]
	v_lshlrev_b32_e32 v251, 1, v250
	v_add_u32_e32 v251, 0xffff8000, v251
	global_load_dword a0, v251, s[100:101]

.LBB0_2396:
	s_or_b64 exec, exec, s[0:1]
	s_barrier
	s_getpc_b64 s[100:101]
	v_min_u32_e32 v251, 0x7d00, v250
	global_load_dword a0, v251, s[100:101]

.LBB0_2762:
	v_readlane_b32 s4, v249, 51
	v_readlane_b32 s5, v249, 52
	s_mov_b64 s[44:45], s[4:5]
	s_cmp_lt_i32 s44, 15
	v_readlane_b32 s6, v249, 53
	v_readlane_b32 s7, v249, 54
	s_cselect_b64 s[0:1], -1, 0
	s_cmp_gt_i32 s45, 15
	s_cselect_b64 s[6:7], -1, 0
	s_and_b64 s[0:1], s[0:1], s[6:7]
	s_andn2_b64 vcc, exec, s[0:1]
	s_cbranch_vccnz .LBB0_2822
	s_waitcnt vmcnt(0)
	s_waitcnt vmcnt(0) lgkmcnt(0)
	s_barrier
	s_cmp_lt_u32 s98, 4
	s_cbranch_scc1 .Lipf_a29
	s_getpc_b64 s[100:101]
	v_lshlrev_b32_e32 v251, 1, v250
	v_add_u32_e32 v251, 0xffff8000, v251
	v_min_u32_e32 v251, 0x3000, v251
	global_load_dword a0, v251, s[100:101]

.LBB0_2821:
	s_or_b64 exec, exec, s[0:1]
	s_barrier
	s_getpc_b64 s[100:101]
	v_min_u32_e32 v251, 0x2600, v250
	global_load_dword a0, v251, s[100:101]

.LBB0_2866:
	s_cmp_gt_i32 s45, 16
	s_cselect_b64 s[0:1], -1, 0
	s_and_b64 s[0:1], s[4:5], s[0:1]
	s_andn2_b64 vcc, exec, s[0:1]
	s_cbranch_vccnz .LBB0_2926
	s_waitcnt vmcnt(0)
	s_waitcnt vmcnt(0) lgkmcnt(0)
	s_barrier
	s_cmp_lt_u32 s98, 4
	s_cbranch_scc1 .Lipf_a31
	s_getpc_b64 s[100:101]
	v_lshlrev_b32_e32 v251, 1, v250
	v_add_u32_e32 v251, 0xffff8000, v251
	v_min_u32_e32 v251, 0xb80, v251
	global_load_dword a0, v251, s[100:101]

	.amdhsa_kernel _Z4mega5MArgs
		.amdhsa_group_segment_fixed_size 0
		.amdhsa_private_segment_fixed_size 0
		.amdhsa_kernarg_size 496
		.amdhsa_user_sgpr_count 2
		.amdhsa_user_sgpr_dispatch_ptr 0
		.amdhsa_user_sgpr_queue_ptr 0
		.amdhsa_user_sgpr_kernarg_segment_ptr 1
		.amdhsa_user_sgpr_dispatch_id 0
		.amdhsa_user_sgpr_kernarg_preload_length 0
		.amdhsa_user_sgpr_kernarg_preload_offset 0
		.amdhsa_user_sgpr_private_segment_size 0
		.amdhsa_uses_dynamic_stack 0
		.amdhsa_enable_private_segment 0
		.amdhsa_system_sgpr_workgroup_id_x 1
		.amdhsa_system_sgpr_workgroup_id_y 0
		.amdhsa_system_sgpr_workgroup_id_z 0
		.amdhsa_system_sgpr_workgroup_info 0
		.amdhsa_system_vgpr_workitem_id 0
		.amdhsa_next_free_vgpr 253
		.amdhsa_next_free_sgpr 102
		.amdhsa_accum_offset 252
		.amdhsa_reserve_vcc 1
		.amdhsa_float_round_mode_32 0
		.amdhsa_float_round_mode_16_64 0
		.amdhsa_float_denorm_mode_32 3
		.amdhsa_float_denorm_mode_16_64 3
		.amdhsa_dx10_clamp 1
		.amdhsa_ieee_mode 1
		.amdhsa_fp16_overflow 0
		.amdhsa_tg_split 0
		.amdhsa_exception_fp_ieee_invalid_op 0
		.amdhsa_exception_fp_denorm_src 0
		.amdhsa_exception_fp_ieee_div_zero 0
		.amdhsa_exception_fp_ieee_overflow 0
		.amdhsa_exception_fp_ieee_underflow 0
		.amdhsa_exception_fp_ieee_inexact 0
		.amdhsa_exception_int_div_zero 0
	.end_amdhsa_kernel

amdhsa.kernels:
  - .agpr_count:     1
    .args:
      - .offset:         0
        .size:           240
        .value_kind:     by_value
      - .offset:         240
        .size:           4
        .value_kind:     hidden_block_count_x
      - .offset:         244
        .size:           4
        .value_kind:     hidden_block_count_y
      - .offset:         248
        .size:           4
        .value_kind:     hidden_block_count_z
      - .offset:         252
        .size:           2
        .value_kind:     hidden_group_size_x
      - .offset:         254
        .size:           2
        .value_kind:     hidden_group_size_y
      - .offset:         256
        .size:           2
        .value_kind:     hidden_group_size_z
      - .offset:         258
        .size:           2
        .value_kind:     hidden_remainder_x
      - .offset:         260
        .size:           2
        .value_kind:     hidden_remainder_y
      - .offset:         262
        .size:           2
        .value_kind:     hidden_remainder_z
      - .offset:         280
        .size:           8
        .value_kind:     hidden_global_offset_x
      - .offset:         288
        .size:           8
        .value_kind:     hidden_global_offset_y
      - .offset:         296
        .size:           8
        .value_kind:     hidden_global_offset_z
      - .offset:         304
        .size:           2
        .value_kind:     hidden_grid_dims
      - .offset:         360
        .size:           4
        .value_kind:     hidden_dynamic_lds_size
    .group_segment_fixed_size: 0
    .kernarg_segment_align: 8
    .kernarg_segment_size: 496
    .language:       OpenCL C
    .language_version:
      - 2
      - 0
    .max_flat_workgroup_size: 512
    .name:           _Z4mega5MArgs
    .private_segment_fixed_size: 0
    .sgpr_count:     108
    .sgpr_spill_count: 65
    .symbol:         _Z4mega5MArgs.kd
    .uniform_work_group_size: 1
    .uses_dynamic_stack: false
    .vgpr_count:     252
    .vgpr_spill_count: 0
    .wavefront_size: 64
